# P5 GEMM epilogue (out = bf16(x+acc)): eight residual-load steps in flight behind counted waits instead of 16 serial load/wait/add/store round trips
# baseline (speedup 1.0000x reference)
; __device__ __forceinline__ unsigned cvt_pk_bf16(float lo, float hi) { unsigned r; asm volatile("v_cvt_pk_bf16_f32 %0, %1, %2" : "=v"(r) : "v"(lo), "v"(hi)); return r; }
;     __device__ __forceinline__ void operator()(const f32x4 (&acc)[2][2][4][2], const Unit& u, int wr, int wc, int fr, int fq) const {
;         const int row0 = u.pm * BM + wr * 64 + fr, col0 = u.pn * BM + wc * 32 + 8 * fq;
; #pragma unroll
;         for (int ai = 0; ai < 2; ++ai)
; #pragma unroll
;             for (int m = 0; m < 4; ++m) { const size_t off = (size_t)(row0 + ai * HALF + m * 16) * ldc + col0;
; #pragma unroll
;                 for (int bj = 0; bj < 2; ++bj) { const f32x4 v0 = *(const f32x4*)(res + off + bj * HALF) + acc[ai][bj][m][0], v1 = *(const f32x4*)(res + off + bj * HALF + 4) + acc[ai][bj][m][1];
;                     u32x4 w; w.x = cvt_pk_bf16(v0[0], v0[1]); w.y = cvt_pk_bf16(v0[2], v0[3]); w.z = cvt_pk_bf16(v1[0], v1[1]); w.w = cvt_pk_bf16(v1[2], v1[3]);
;                     *(u32x4*)(out + off + bj * HALF) = w; }
;                 if (m & 1) asm volatile("" ::: "memory"); }
;     }
.LBB0_545:
	v_lshl_add_u32 v152, s30, 8, v155
	v_lshl_or_b32 v150, s53, 8, v157
	s_andn2_b64 vcc, exec, s[4:5]
	s_mov_b64 s[4:5], -1
	v_ashrrev_i32_e32 v153, 31, v152
	v_ashrrev_i32_e32 v151, 31, v150
	v_lshlrev_b64 v[148:149], 12, v[152:153]
	v_lshl_add_u64 v[148:149], v[148:149], 0, v[150:151]
	v_lshl_add_u64 v[162:163], v[148:149], 2, s[64:65]
	v_lshl_add_u64 v[164:165], v[148:149], 1, s[8:9]
	s_mov_b64 s[80:81], 0x40000
	s_mov_b64 s[82:83], 0x140000
	s_mov_b64 s[84:85], 0x20000
	s_mov_b64 s[86:87], 0xa0000
	global_load_dwordx4 v[170:173], v[162:163], off
	global_load_dwordx4 v[174:177], v[162:163], off offset:16
	global_load_dwordx4 v[178:181], v[162:163], off offset:512
	global_load_dwordx4 v[182:185], v[162:163], off offset:528
	v_lshl_add_u64 v[162:163], v[162:163], 0, s[80:81]
	global_load_dwordx4 v[186:189], v[162:163], off
	global_load_dwordx4 v[190:193], v[162:163], off offset:16
	global_load_dwordx4 v[194:197], v[162:163], off offset:512
	global_load_dwordx4 v[198:201], v[162:163], off offset:528
	v_lshl_add_u64 v[162:163], v[162:163], 0, s[80:81]
	global_load_dwordx4 v[202:205], v[162:163], off
	global_load_dwordx4 v[206:209], v[162:163], off offset:16
	global_load_dwordx4 v[210:213], v[162:163], off offset:512
	global_load_dwordx4 v[214:217], v[162:163], off offset:528
	v_lshl_add_u64 v[162:163], v[162:163], 0, s[80:81]
	global_load_dwordx4 v[218:221], v[162:163], off
	global_load_dwordx4 v[222:225], v[162:163], off offset:16
	global_load_dwordx4 v[246:249], v[162:163], off offset:512
	global_load_dwordx4 v[250:253], v[162:163], off offset:528
	v_lshl_add_u64 v[162:163], v[162:163], 0, s[82:83]
	s_waitcnt vmcnt(14)
	v_pk_add_f32 v[126:127], v[126:127], v[170:171]
	v_pk_add_f32 v[128:129], v[128:129], v[172:173]
	v_pk_add_f32 v[174:175], v[122:123], v[174:175]
	v_pk_add_f32 v[176:177], v[124:125], v[176:177]
	v_cvt_pk_bf16_f32 v122, v126, v127
	v_cvt_pk_bf16_f32 v123, v128, v129
	v_cvt_pk_bf16_f32 v124, v174, v175
	v_cvt_pk_bf16_f32 v125, v176, v177
	global_store_dwordx4 v[164:165], v[122:125], off
	global_load_dwordx4 v[170:173], v[162:163], off
	global_load_dwordx4 v[174:177], v[162:163], off offset:16
	s_waitcnt vmcnt(15)
	v_pk_add_f32 v[118:119], v[118:119], v[178:179]
	v_pk_add_f32 v[120:121], v[120:121], v[180:181]
	v_pk_add_f32 v[182:183], v[114:115], v[182:183]
	v_pk_add_f32 v[184:185], v[116:117], v[184:185]
	v_cvt_pk_bf16_f32 v114, v118, v119
	v_cvt_pk_bf16_f32 v115, v120, v121
	v_cvt_pk_bf16_f32 v116, v182, v183
	v_cvt_pk_bf16_f32 v117, v184, v185
	global_store_dwordx4 v[164:165], v[114:117], off offset:256
	v_lshl_add_u64 v[164:165], v[164:165], 0, s[84:85]
	global_load_dwordx4 v[178:181], v[162:163], off offset:512
	global_load_dwordx4 v[182:185], v[162:163], off offset:528
	v_lshl_add_u64 v[162:163], v[162:163], 0, s[80:81]
	s_waitcnt vmcnt(16)
	v_pk_add_f32 v[110:111], v[110:111], v[186:187]
	v_pk_add_f32 v[112:113], v[112:113], v[188:189]
	v_pk_add_f32 v[190:191], v[106:107], v[190:191]
	v_pk_add_f32 v[192:193], v[108:109], v[192:193]
	v_cvt_pk_bf16_f32 v106, v110, v111
	v_cvt_pk_bf16_f32 v107, v112, v113
	v_cvt_pk_bf16_f32 v108, v190, v191
	v_cvt_pk_bf16_f32 v109, v192, v193
	global_store_dwordx4 v[164:165], v[106:109], off
	global_load_dwordx4 v[186:189], v[162:163], off
	global_load_dwordx4 v[190:193], v[162:163], off offset:16
	s_waitcnt vmcnt(17)
	v_pk_add_f32 v[102:103], v[102:103], v[194:195]
	v_pk_add_f32 v[104:105], v[104:105], v[196:197]
	v_pk_add_f32 v[198:199], v[98:99], v[198:199]
	v_pk_add_f32 v[200:201], v[100:101], v[200:201]
	v_cvt_pk_bf16_f32 v98, v102, v103
	v_cvt_pk_bf16_f32 v99, v104, v105
	v_cvt_pk_bf16_f32 v100, v198, v199
	v_cvt_pk_bf16_f32 v101, v200, v201
	global_store_dwordx4 v[164:165], v[98:101], off offset:256
	v_lshl_add_u64 v[164:165], v[164:165], 0, s[84:85]
	global_load_dwordx4 v[194:197], v[162:163], off offset:512
	global_load_dwordx4 v[198:201], v[162:163], off offset:528
	v_lshl_add_u64 v[162:163], v[162:163], 0, s[80:81]
	s_waitcnt vmcnt(18)
	v_pk_add_f32 v[94:95], v[94:95], v[202:203]
	v_pk_add_f32 v[96:97], v[96:97], v[204:205]
	v_pk_add_f32 v[206:207], v[90:91], v[206:207]
	v_pk_add_f32 v[208:209], v[92:93], v[208:209]
	v_cvt_pk_bf16_f32 v90, v94, v95
	v_cvt_pk_bf16_f32 v91, v96, v97
	v_cvt_pk_bf16_f32 v92, v206, v207
	v_cvt_pk_bf16_f32 v93, v208, v209
	global_store_dwordx4 v[164:165], v[90:93], off
	global_load_dwordx4 v[202:205], v[162:163], off
	global_load_dwordx4 v[206:209], v[162:163], off offset:16
	s_waitcnt vmcnt(19)
; __device__ __forceinline__ unsigned cvt_pk_bf16(float lo, float hi) { unsigned r; asm volatile("v_cvt_pk_bf16_f32 %0, %1, %2" : "=v"(r) : "v"(lo), "v"(hi)); return r; }
;     __device__ __forceinline__ void operator()(const f32x4 (&acc)[2][2][4][2], const Unit& u, int wr, int wc, int fr, int fq) const {
;         const int row0 = u.pm * BM + wr * 64 + fr, col0 = u.pn * BM + wc * 32 + 8 * fq;
; #pragma unroll
;         for (int ai = 0; ai < 2; ++ai)
; #pragma unroll
;             for (int m = 0; m < 4; ++m) { const size_t off = (size_t)(row0 + ai * HALF + m * 16) * ldc + col0;
; #pragma unroll
;                 for (int bj = 0; bj < 2; ++bj) { const f32x4 v0 = *(const f32x4*)(res + off + bj * HALF) + acc[ai][bj][m][0], v1 = *(const f32x4*)(res + off + bj * HALF + 4) + acc[ai][bj][m][1];
;                     u32x4 w; w.x = cvt_pk_bf16(v0[0], v0[1]); w.y = cvt_pk_bf16(v0[2], v0[3]); w.z = cvt_pk_bf16(v1[0], v1[1]); w.w = cvt_pk_bf16(v1[2], v1[3]);
;                     *(u32x4*)(out + off + bj * HALF) = w; }
;                 if (m & 1) asm volatile("" ::: "memory"); }
;     }
	v_pk_add_f32 v[86:87], v[86:87], v[210:211]
	v_pk_add_f32 v[88:89], v[88:89], v[212:213]
	v_pk_add_f32 v[214:215], v[82:83], v[214:215]
	v_pk_add_f32 v[216:217], v[84:85], v[216:217]
	v_cvt_pk_bf16_f32 v82, v86, v87
	v_cvt_pk_bf16_f32 v83, v88, v89
	v_cvt_pk_bf16_f32 v84, v214, v215
	v_cvt_pk_bf16_f32 v85, v216, v217
	global_store_dwordx4 v[164:165], v[82:85], off offset:256
	v_lshl_add_u64 v[164:165], v[164:165], 0, s[84:85]
	global_load_dwordx4 v[210:213], v[162:163], off offset:512
	global_load_dwordx4 v[214:217], v[162:163], off offset:528
	v_lshl_add_u64 v[162:163], v[162:163], 0, s[80:81]
	s_waitcnt vmcnt(20)
	v_pk_add_f32 v[78:79], v[78:79], v[218:219]
	v_pk_add_f32 v[80:81], v[80:81], v[220:221]
	v_pk_add_f32 v[222:223], v[74:75], v[222:223]
	v_pk_add_f32 v[224:225], v[76:77], v[224:225]
	v_cvt_pk_bf16_f32 v74, v78, v79
	v_cvt_pk_bf16_f32 v75, v80, v81
	v_cvt_pk_bf16_f32 v76, v222, v223
	v_cvt_pk_bf16_f32 v77, v224, v225
	global_store_dwordx4 v[164:165], v[74:77], off
	global_load_dwordx4 v[218:221], v[162:163], off
	global_load_dwordx4 v[222:225], v[162:163], off offset:16
	s_waitcnt vmcnt(21)
	v_pk_add_f32 v[70:71], v[70:71], v[246:247]
	v_pk_add_f32 v[72:73], v[72:73], v[248:249]
	v_pk_add_f32 v[250:251], v[66:67], v[250:251]
	v_pk_add_f32 v[252:253], v[68:69], v[252:253]
	v_cvt_pk_bf16_f32 v66, v70, v71
	v_cvt_pk_bf16_f32 v67, v72, v73
	v_cvt_pk_bf16_f32 v68, v250, v251
	v_cvt_pk_bf16_f32 v69, v252, v253
	global_store_dwordx4 v[164:165], v[66:69], off offset:256
	v_lshl_add_u64 v[164:165], v[164:165], 0, s[86:87]
	global_load_dwordx4 v[246:249], v[162:163], off offset:512
	global_load_dwordx4 v[250:253], v[162:163], off offset:528
	s_waitcnt vmcnt(21)
	v_pk_add_f32 v[62:63], v[62:63], v[170:171]
	v_pk_add_f32 v[64:65], v[64:65], v[172:173]
	v_pk_add_f32 v[174:175], v[58:59], v[174:175]
	v_pk_add_f32 v[176:177], v[60:61], v[176:177]
	v_cvt_pk_bf16_f32 v58, v62, v63
	v_cvt_pk_bf16_f32 v59, v64, v65
	v_cvt_pk_bf16_f32 v60, v174, v175
	v_cvt_pk_bf16_f32 v61, v176, v177
	global_store_dwordx4 v[164:165], v[58:61], off
	s_waitcnt vmcnt(19)
	v_pk_add_f32 v[54:55], v[54:55], v[178:179]
	v_pk_add_f32 v[56:57], v[56:57], v[180:181]
	v_pk_add_f32 v[182:183], v[50:51], v[182:183]
	v_pk_add_f32 v[184:185], v[52:53], v[184:185]
	v_cvt_pk_bf16_f32 v50, v54, v55
	v_cvt_pk_bf16_f32 v51, v56, v57
	v_cvt_pk_bf16_f32 v52, v182, v183
	v_cvt_pk_bf16_f32 v53, v184, v185
	global_store_dwordx4 v[164:165], v[50:53], off offset:256
	v_lshl_add_u64 v[164:165], v[164:165], 0, s[84:85]
	s_waitcnt vmcnt(17)
	v_pk_add_f32 v[46:47], v[46:47], v[186:187]
	v_pk_add_f32 v[48:49], v[48:49], v[188:189]
	v_pk_add_f32 v[190:191], v[42:43], v[190:191]
	v_pk_add_f32 v[192:193], v[44:45], v[192:193]
	v_cvt_pk_bf16_f32 v42, v46, v47
	v_cvt_pk_bf16_f32 v43, v48, v49
	v_cvt_pk_bf16_f32 v44, v190, v191
	v_cvt_pk_bf16_f32 v45, v192, v193
	global_store_dwordx4 v[164:165], v[42:45], off
	s_waitcnt vmcnt(15)
	v_pk_add_f32 v[38:39], v[38:39], v[194:195]
	v_pk_add_f32 v[40:41], v[40:41], v[196:197]
	v_pk_add_f32 v[198:199], v[34:35], v[198:199]
	v_pk_add_f32 v[200:201], v[36:37], v[200:201]
	v_cvt_pk_bf16_f32 v34, v38, v39
	v_cvt_pk_bf16_f32 v35, v40, v41
	v_cvt_pk_bf16_f32 v36, v198, v199
	v_cvt_pk_bf16_f32 v37, v200, v201
	global_store_dwordx4 v[164:165], v[34:37], off offset:256
	v_lshl_add_u64 v[164:165], v[164:165], 0, s[84:85]
	s_waitcnt vmcnt(13)
	v_pk_add_f32 v[30:31], v[30:31], v[202:203]
	v_pk_add_f32 v[32:33], v[32:33], v[204:205]
	v_pk_add_f32 v[206:207], v[26:27], v[206:207]
	v_pk_add_f32 v[208:209], v[28:29], v[208:209]
	v_cvt_pk_bf16_f32 v26, v30, v31
	v_cvt_pk_bf16_f32 v27, v32, v33
	v_cvt_pk_bf16_f32 v28, v206, v207
	v_cvt_pk_bf16_f32 v29, v208, v209
	global_store_dwordx4 v[164:165], v[26:29], off
	s_waitcnt vmcnt(11)
	v_pk_add_f32 v[22:23], v[22:23], v[210:211]
	v_pk_add_f32 v[24:25], v[24:25], v[212:213]
	v_pk_add_f32 v[214:215], v[18:19], v[214:215]
	v_pk_add_f32 v[216:217], v[20:21], v[216:217]
	v_cvt_pk_bf16_f32 v18, v22, v23
	v_cvt_pk_bf16_f32 v19, v24, v25
	v_cvt_pk_bf16_f32 v20, v214, v215
	v_cvt_pk_bf16_f32 v21, v216, v217
	global_store_dwordx4 v[164:165], v[18:21], off offset:256
	v_lshl_add_u64 v[164:165], v[164:165], 0, s[84:85]
	s_waitcnt vmcnt(9)
	v_pk_add_f32 v[14:15], v[14:15], v[218:219]
	v_pk_add_f32 v[16:17], v[16:17], v[220:221]
	v_pk_add_f32 v[222:223], v[10:11], v[222:223]
	v_pk_add_f32 v[224:225], v[12:13], v[224:225]
	v_cvt_pk_bf16_f32 v10, v14, v15
	v_cvt_pk_bf16_f32 v11, v16, v17
	v_cvt_pk_bf16_f32 v12, v222, v223
	v_cvt_pk_bf16_f32 v13, v224, v225
	global_store_dwordx4 v[164:165], v[10:13], off
	s_waitcnt vmcnt(7)
	v_pk_add_f32 v[6:7], v[6:7], v[246:247]
	v_pk_add_f32 v[8:9], v[8:9], v[248:249]
	v_pk_add_f32 v[250:251], v[2:3], v[250:251]
	v_pk_add_f32 v[252:253], v[4:5], v[252:253]
	v_cvt_pk_bf16_f32 v2, v6, v7
	v_cvt_pk_bf16_f32 v3, v8, v9
	v_cvt_pk_bf16_f32 v4, v250, v251
	v_cvt_pk_bf16_f32 v5, v252, v253
	global_store_dwordx4 v[164:165], v[2:5], off offset:256
	s_cbranch_vccnz .LBB0_534
	s_andn2_b64 vcc, exec, s[6:7]
	s_cbranch_vccnz .LBB0_533
	s_barrier
	s_branch .LBB0_533
